# P9 epilogue ACT stores nt (on top of P1 nt)
# baseline (speedup 1.0000x reference)
.LBB0_1114:
	s_lshl_b32 s23, s59, 2
	s_add_i32 s68, s68, s23
	s_nop 15
	s_nop 15
	v_add_u32_e32 v2, s68, v209
	ds_read_b128 v[14:17], v2
	ds_read_b128 v[6:9], v2 offset:16
	ds_read_b128 v[10:13], v2 offset:512
	ds_read_b128 v[2:5], v2 offset:528
	v_lshl_add_u32 v18, s67, 8, v233
	s_waitcnt lgkmcnt(0)
	v_pk_add_f32 v[22:23], v[102:103], v[14:15]
	v_pk_add_f32 v[20:21], v[104:105], v[16:17]
	v_min_f32_e32 v22, 0x40e00000, v22
	v_min_f32_e32 v23, 0x40e00000, v23
	v_pk_mul_f32 v[26:27], v[22:23], s[18:19] op_sel_hi:[1,0]
	v_min_f32_e32 v20, 0x40e00000, v20
	v_exp_f32_e32 v26, v26
	v_exp_f32_e32 v27, v27
	v_min_f32_e32 v21, 0x40e00000, v21
	v_pk_mul_f32 v[30:31], v[20:21], s[18:19] op_sel_hi:[1,0]
	v_pk_add_f32 v[28:29], v[162:163], v[10:11]
	v_pk_add_f32 v[26:27], v[26:27], 1.0 op_sel_hi:[1,0]
	v_exp_f32_e32 v30, v30
	v_rcp_f32_e32 v26, v26
	v_rcp_f32_e32 v27, v27
	v_exp_f32_e32 v31, v31
	v_med3_f32 v28, v28, s66, v239
	v_med3_f32 v29, v29, s66, v239
	v_pk_fma_f32 v[28:29], v[28:29], 4.0, 4.0 op_sel_hi:[1,0,0]
	v_pk_add_f32 v[24:25], v[164:165], v[12:13]
	v_pk_mul_f32 v[22:23], v[22:23], v[28:29]
	v_med3_f32 v24, v24, s66, v239
	v_pk_mul_f32 v[22:23], v[22:23], v[26:27]
	v_pk_add_f32 v[26:27], v[30:31], 1.0 op_sel_hi:[1,0]
	v_med3_f32 v25, v25, s66, v239
	v_rcp_f32_e32 v26, v26
	v_rcp_f32_e32 v27, v27
	v_pk_fma_f32 v[24:25], v[24:25], 4.0, 4.0 op_sel_hi:[1,0,0]
	v_pk_add_f32 v[32:33], v[166:167], v[2:3]
	v_pk_mul_f32 v[20:21], v[20:21], v[24:25]
	v_med3_f32 v32, v32, s66, v239
	v_pk_mul_f32 v[24:25], v[20:21], v[26:27]
	v_pk_add_f32 v[26:27], v[110:111], v[6:7]
	v_med3_f32 v33, v33, s66, v239
	v_min_f32_e32 v26, 0x40e00000, v26
	v_min_f32_e32 v27, 0x40e00000, v27
	v_pk_mul_f32 v[30:31], v[26:27], s[18:19] op_sel_hi:[1,0]
	v_pk_add_f32 v[20:21], v[112:113], v[8:9]
	v_exp_f32_e32 v30, v30
	v_exp_f32_e32 v31, v31
	v_pk_fma_f32 v[32:33], v[32:33], 4.0, 4.0 op_sel_hi:[1,0,0]
	v_pk_add_f32 v[28:29], v[168:169], v[4:5]
	v_pk_mul_f32 v[26:27], v[26:27], v[32:33]
	v_min_f32_e32 v32, 0x40e00000, v20
	v_min_f32_e32 v33, 0x40e00000, v21
	v_pk_mul_f32 v[20:21], v[32:33], s[18:19] op_sel_hi:[1,0]
	v_pk_add_f32 v[30:31], v[30:31], 1.0 op_sel_hi:[1,0]
	v_exp_f32_e32 v20, v20
	v_exp_f32_e32 v21, v21
	v_rcp_f32_e32 v30, v30
	v_rcp_f32_e32 v31, v31
	v_med3_f32 v28, v28, s66, v239
	v_pk_add_f32 v[20:21], v[20:21], 1.0 op_sel_hi:[1,0]
	v_med3_f32 v29, v29, s66, v239
	v_pk_mul_f32 v[26:27], v[26:27], v[30:31]
	v_rcp_f32_e32 v30, v20
	v_mov_b32_e32 v20, v199
	v_cvt_pk_fp8_f32 v20, v22, v23
	v_rcp_f32_e32 v31, v21
	v_mov_b32_e32 v21, v199
	v_pk_fma_f32 v[28:29], v[28:29], 4.0, 4.0 op_sel_hi:[1,0,0]
	v_cvt_pk_fp8_f32 v20, v24, v25 op_sel:[0,0,1]
	v_pk_add_f32 v[24:25], v[122:123], v[14:15]
	v_cvt_pk_fp8_f32 v21, v26, v27
	v_min_f32_e32 v24, 0x40e00000, v24
	v_min_f32_e32 v25, 0x40e00000, v25
	v_pk_mul_f32 v[22:23], v[32:33], v[28:29]
	v_pk_mul_f32 v[28:29], v[24:25], s[18:19] op_sel_hi:[1,0]
	v_pk_mul_f32 v[22:23], v[22:23], v[30:31]
	v_exp_f32_e32 v28, v28
	v_exp_f32_e32 v29, v29
	v_cvt_pk_fp8_f32 v21, v22, v23 op_sel:[0,0,1]
	v_pk_add_f32 v[22:23], v[124:125], v[16:17]
	v_pk_add_f32 v[30:31], v[170:171], v[10:11]
	v_min_f32_e32 v22, 0x40e00000, v22
	v_min_f32_e32 v23, 0x40e00000, v23
	v_pk_add_f32 v[28:29], v[28:29], 1.0 op_sel_hi:[1,0]
	v_pk_mul_f32 v[32:33], v[22:23], s[18:19] op_sel_hi:[1,0]
	v_rcp_f32_e32 v28, v28
	v_rcp_f32_e32 v29, v29
	v_exp_f32_e32 v32, v32
	v_exp_f32_e32 v33, v33
	v_med3_f32 v30, v30, s66, v239
	v_med3_f32 v31, v31, s66, v239
	v_pk_fma_f32 v[30:31], v[30:31], 4.0, 4.0 op_sel_hi:[1,0,0]
	v_pk_add_f32 v[26:27], v[172:173], v[12:13]
	v_pk_mul_f32 v[24:25], v[24:25], v[30:31]
	v_med3_f32 v26, v26, s66, v239
	v_pk_mul_f32 v[24:25], v[24:25], v[28:29]
	v_pk_add_f32 v[28:29], v[32:33], 1.0 op_sel_hi:[1,0]
	v_med3_f32 v27, v27, s66, v239
	v_rcp_f32_e32 v28, v28
	v_rcp_f32_e32 v29, v29
	v_pk_fma_f32 v[26:27], v[26:27], 4.0, 4.0 op_sel_hi:[1,0,0]
	v_pk_add_f32 v[34:35], v[174:175], v[2:3]
	v_pk_mul_f32 v[22:23], v[22:23], v[26:27]
	v_med3_f32 v34, v34, s66, v239
	v_pk_mul_f32 v[26:27], v[22:23], v[28:29]
	v_pk_add_f32 v[28:29], v[130:131], v[6:7]
	v_med3_f32 v35, v35, s66, v239
	v_min_f32_e32 v28, 0x40e00000, v28
	v_min_f32_e32 v29, 0x40e00000, v29
	v_pk_mul_f32 v[32:33], v[28:29], s[18:19] op_sel_hi:[1,0]
	v_pk_add_f32 v[22:23], v[132:133], v[8:9]
	v_exp_f32_e32 v32, v32
	v_exp_f32_e32 v33, v33
	v_pk_fma_f32 v[34:35], v[34:35], 4.0, 4.0 op_sel_hi:[1,0,0]
	v_pk_add_f32 v[30:31], v[176:177], v[4:5]
	v_pk_mul_f32 v[28:29], v[28:29], v[34:35]
	v_min_f32_e32 v34, 0x40e00000, v22
	v_min_f32_e32 v35, 0x40e00000, v23
	v_pk_mul_f32 v[22:23], v[34:35], s[18:19] op_sel_hi:[1,0]
	v_pk_add_f32 v[32:33], v[32:33], 1.0 op_sel_hi:[1,0]
	v_exp_f32_e32 v22, v22
	v_exp_f32_e32 v23, v23
	v_rcp_f32_e32 v32, v32
	v_rcp_f32_e32 v33, v33
	v_med3_f32 v30, v30, s66, v239
	v_pk_add_f32 v[22:23], v[22:23], 1.0 op_sel_hi:[1,0]
	v_med3_f32 v31, v31, s66, v239
	v_pk_mul_f32 v[28:29], v[28:29], v[32:33]
	v_rcp_f32_e32 v32, v22
	v_rcp_f32_e32 v33, v23
	v_mov_b32_e32 v22, v199
	v_mov_b32_e32 v23, v199
	v_cvt_pk_fp8_f32 v22, v24, v25
	v_cvt_pk_fp8_f32 v23, v28, v29
	v_pk_fma_f32 v[30:31], v[30:31], 4.0, 4.0 op_sel_hi:[1,0,0]
	s_lshl_b32 s21, s28, 7
	v_pk_mul_f32 v[24:25], v[34:35], v[30:31]
	v_cvt_pk_fp8_f32 v22, v26, v27 op_sel:[0,0,1]
	v_pk_mul_f32 v[24:25], v[24:25], v[32:33]
	v_ashrrev_i32_e32 v19, 31, v18
	v_cvt_pk_fp8_f32 v23, v24, v25 op_sel:[0,0,1]
	s_and_b32 s21, s21, 0x380
	v_lshlrev_b64 v[24:25], 10, v[18:19]
	v_or_b32_e32 v198, s21, v234
	v_lshl_add_u64 v[24:25], s[8:9], 0, v[24:25]
	v_permlane16_swap_b32_e32 v20, v22
	v_permlane16_swap_b32_e32 v21, v23
	v_lshl_add_u64 v[24:25], v[24:25], 0, v[198:199]
	global_store_dwordx4 v[24:25], v[20:23], off nt
	v_pk_add_f32 v[28:29], v[178:179], v[10:11]
	v_pk_add_f32 v[24:25], v[180:181], v[12:13]
	v_pk_add_f32 v[22:23], v[142:143], v[14:15]
	v_pk_add_f32 v[20:21], v[144:145], v[16:17]
	v_min_f32_e32 v22, 0x40e00000, v22
	v_min_f32_e32 v23, 0x40e00000, v23
	v_pk_mul_f32 v[26:27], v[22:23], s[18:19] op_sel_hi:[1,0]
	v_min_f32_e32 v20, 0x40e00000, v20
	v_exp_f32_e32 v26, v26
	v_exp_f32_e32 v27, v27
	v_min_f32_e32 v21, 0x40e00000, v21
	v_pk_mul_f32 v[30:31], v[20:21], s[18:19] op_sel_hi:[1,0]
	v_med3_f32 v28, v28, s66, v239
	v_pk_add_f32 v[26:27], v[26:27], 1.0 op_sel_hi:[1,0]
	v_exp_f32_e32 v30, v30
	v_rcp_f32_e32 v26, v26
	v_rcp_f32_e32 v27, v27
	v_exp_f32_e32 v31, v31
	v_med3_f32 v29, v29, s66, v239
	v_pk_fma_f32 v[28:29], v[28:29], 4.0, 4.0 op_sel_hi:[1,0,0]
	v_med3_f32 v24, v24, s66, v239
	v_pk_mul_f32 v[22:23], v[22:23], v[28:29]
	v_med3_f32 v25, v25, s66, v239
	v_pk_mul_f32 v[22:23], v[22:23], v[26:27]
	v_pk_add_f32 v[26:27], v[30:31], 1.0 op_sel_hi:[1,0]
	v_pk_fma_f32 v[24:25], v[24:25], 4.0, 4.0 op_sel_hi:[1,0,0]
	v_rcp_f32_e32 v26, v26
	v_rcp_f32_e32 v27, v27
	v_pk_mul_f32 v[20:21], v[20:21], v[24:25]
	v_pk_add_f32 v[32:33], v[182:183], v[2:3]
	v_pk_add_f32 v[28:29], v[184:185], v[4:5]
	v_pk_mul_f32 v[24:25], v[20:21], v[26:27]
	v_pk_add_f32 v[26:27], v[150:151], v[6:7]
	v_med3_f32 v32, v32, s66, v239
	v_min_f32_e32 v26, 0x40e00000, v26
	v_min_f32_e32 v27, 0x40e00000, v27
	v_pk_mul_f32 v[30:31], v[26:27], s[18:19] op_sel_hi:[1,0]
	v_med3_f32 v33, v33, s66, v239
	v_exp_f32_e32 v30, v30
	v_exp_f32_e32 v31, v31
	v_pk_add_f32 v[20:21], v[152:153], v[8:9]
	v_pk_fma_f32 v[32:33], v[32:33], 4.0, 4.0 op_sel_hi:[1,0,0]
	v_med3_f32 v28, v28, s66, v239
	v_pk_mul_f32 v[26:27], v[26:27], v[32:33]
	v_min_f32_e32 v32, 0x40e00000, v20
	v_min_f32_e32 v33, 0x40e00000, v21
	v_pk_mul_f32 v[20:21], v[32:33], s[18:19] op_sel_hi:[1,0]
	v_pk_add_f32 v[30:31], v[30:31], 1.0 op_sel_hi:[1,0]
	v_exp_f32_e32 v20, v20
	v_exp_f32_e32 v21, v21
	v_rcp_f32_e32 v30, v30
	v_rcp_f32_e32 v31, v31
	v_med3_f32 v29, v29, s66, v239
	v_pk_add_f32 v[20:21], v[20:21], 1.0 op_sel_hi:[1,0]
	v_pk_fma_f32 v[28:29], v[28:29], 4.0, 4.0 op_sel_hi:[1,0,0]
	v_pk_mul_f32 v[26:27], v[26:27], v[30:31]
	v_rcp_f32_e32 v30, v20
	v_mov_b32_e32 v20, v199
	v_cvt_pk_fp8_f32 v20, v22, v23
	v_rcp_f32_e32 v31, v21
	v_mov_b32_e32 v21, v199
	v_cvt_pk_fp8_f32 v21, v26, v27
	v_cvt_pk_fp8_f32 v20, v24, v25 op_sel:[0,0,1]
	v_pk_add_f32 v[24:25], v[154:155], v[14:15]
	v_pk_mul_f32 v[22:23], v[32:33], v[28:29]
	v_min_f32_e32 v24, 0x40e00000, v24
	v_min_f32_e32 v25, 0x40e00000, v25
	v_pk_mul_f32 v[28:29], v[24:25], s[18:19] op_sel_hi:[1,0]
	v_pk_mul_f32 v[22:23], v[22:23], v[30:31]
	v_exp_f32_e32 v28, v28
	v_exp_f32_e32 v29, v29
	v_cvt_pk_fp8_f32 v21, v22, v23 op_sel:[0,0,1]
	v_pk_add_f32 v[22:23], v[156:157], v[16:17]
	v_pk_add_f32 v[30:31], v[186:187], v[10:11]
	v_min_f32_e32 v22, 0x40e00000, v22
	v_min_f32_e32 v23, 0x40e00000, v23
	v_pk_add_f32 v[28:29], v[28:29], 1.0 op_sel_hi:[1,0]
	v_pk_mul_f32 v[32:33], v[22:23], s[18:19] op_sel_hi:[1,0]
	v_rcp_f32_e32 v28, v28
	v_rcp_f32_e32 v29, v29
	v_exp_f32_e32 v32, v32
	v_exp_f32_e32 v33, v33
	v_med3_f32 v30, v30, s66, v239
	v_med3_f32 v31, v31, s66, v239
	v_pk_fma_f32 v[30:31], v[30:31], 4.0, 4.0 op_sel_hi:[1,0,0]
	v_pk_add_f32 v[26:27], v[188:189], v[12:13]
	v_pk_mul_f32 v[24:25], v[24:25], v[30:31]
	v_med3_f32 v26, v26, s66, v239
	v_pk_mul_f32 v[24:25], v[24:25], v[28:29]
	v_pk_add_f32 v[28:29], v[32:33], 1.0 op_sel_hi:[1,0]
	v_med3_f32 v27, v27, s66, v239
	v_rcp_f32_e32 v28, v28
	v_rcp_f32_e32 v29, v29
	v_pk_fma_f32 v[26:27], v[26:27], 4.0, 4.0 op_sel_hi:[1,0,0]
	v_pk_add_f32 v[34:35], v[190:191], v[2:3]
	v_pk_mul_f32 v[22:23], v[22:23], v[26:27]
	v_med3_f32 v34, v34, s66, v239
	v_pk_mul_f32 v[26:27], v[22:23], v[28:29]
	v_pk_add_f32 v[28:29], v[158:159], v[6:7]
	v_med3_f32 v35, v35, s66, v239
	v_min_f32_e32 v28, 0x40e00000, v28
	v_min_f32_e32 v29, 0x40e00000, v29
	v_pk_mul_f32 v[32:33], v[28:29], s[18:19] op_sel_hi:[1,0]
	v_pk_add_f32 v[22:23], v[160:161], v[8:9]
	v_exp_f32_e32 v32, v32
	v_exp_f32_e32 v33, v33
	v_pk_fma_f32 v[34:35], v[34:35], 4.0, 4.0 op_sel_hi:[1,0,0]
	v_pk_add_f32 v[30:31], v[192:193], v[4:5]
	v_pk_mul_f32 v[28:29], v[28:29], v[34:35]
	v_min_f32_e32 v34, 0x40e00000, v22
	v_min_f32_e32 v35, 0x40e00000, v23
	v_pk_mul_f32 v[22:23], v[34:35], s[18:19] op_sel_hi:[1,0]
	v_pk_add_f32 v[32:33], v[32:33], 1.0 op_sel_hi:[1,0]
	v_exp_f32_e32 v22, v22
	v_exp_f32_e32 v23, v23
	v_rcp_f32_e32 v32, v32
	v_rcp_f32_e32 v33, v33
	v_med3_f32 v30, v30, s66, v239
	v_pk_add_f32 v[22:23], v[22:23], 1.0 op_sel_hi:[1,0]
	v_med3_f32 v31, v31, s66, v239
	v_pk_mul_f32 v[28:29], v[28:29], v[32:33]
	v_rcp_f32_e32 v32, v22
	v_rcp_f32_e32 v33, v23
	v_mov_b32_e32 v22, v199
	v_mov_b32_e32 v23, v199
	v_cvt_pk_fp8_f32 v22, v24, v25
	v_cvt_pk_fp8_f32 v23, v28, v29
	v_pk_fma_f32 v[30:31], v[30:31], 4.0, 4.0 op_sel_hi:[1,0,0]
	v_pk_add_f32 v[36:37], v[118:119], v[2:3]
	v_pk_mul_f32 v[24:25], v[34:35], v[30:31]
	v_cvt_pk_fp8_f32 v22, v26, v27 op_sel:[0,0,1]
	v_pk_mul_f32 v[24:25], v[24:25], v[32:33]
	v_pk_add_f32 v[30:31], v[98:99], v[10:11]
	v_cvt_pk_fp8_f32 v23, v24, v25 op_sel:[0,0,1]
	v_or_b32_e32 v24, 32, v18
	v_ashrrev_i32_e32 v25, 31, v24
	v_lshlrev_b64 v[24:25], 10, v[24:25]
	v_lshl_add_u64 v[24:25], s[8:9], 0, v[24:25]
	v_permlane16_swap_b32_e32 v20, v22
	v_permlane16_swap_b32_e32 v21, v23
	v_lshl_add_u64 v[24:25], v[24:25], 0, v[198:199]
	global_store_dwordx4 v[24:25], v[20:23], off nt
	v_pk_add_f32 v[24:25], v[66:67], v[14:15]
	v_med3_f32 v30, v30, s66, v239
	v_min_f32_e32 v24, 0x40e00000, v24
	v_min_f32_e32 v25, 0x40e00000, v25
	v_pk_mul_f32 v[28:29], v[24:25], s[18:19] op_sel_hi:[1,0]
	v_pk_add_f32 v[22:23], v[68:69], v[16:17]
	v_exp_f32_e32 v28, v28
	v_exp_f32_e32 v29, v29
	v_min_f32_e32 v22, 0x40e00000, v22
	v_min_f32_e32 v23, 0x40e00000, v23
	v_pk_mul_f32 v[32:33], v[22:23], s[18:19] op_sel_hi:[1,0]
	v_pk_add_f32 v[28:29], v[28:29], 1.0 op_sel_hi:[1,0]
	v_exp_f32_e32 v32, v32
	v_rcp_f32_e32 v28, v28
	v_rcp_f32_e32 v29, v29
	v_exp_f32_e32 v33, v33
	v_med3_f32 v31, v31, s66, v239
	v_pk_fma_f32 v[30:31], v[30:31], 4.0, 4.0 op_sel_hi:[1,0,0]
	v_pk_add_f32 v[26:27], v[100:101], v[12:13]
	v_pk_mul_f32 v[24:25], v[24:25], v[30:31]
	v_med3_f32 v26, v26, s66, v239
	v_pk_mul_f32 v[24:25], v[24:25], v[28:29]
	v_pk_add_f32 v[28:29], v[32:33], 1.0 op_sel_hi:[1,0]
	v_med3_f32 v27, v27, s66, v239
	v_rcp_f32_e32 v28, v28
	v_rcp_f32_e32 v29, v29
	v_pk_fma_f32 v[26:27], v[26:27], 4.0, 4.0 op_sel_hi:[1,0,0]
	v_pk_add_f32 v[34:35], v[106:107], v[2:3]
	v_pk_mul_f32 v[22:23], v[22:23], v[26:27]
	v_med3_f32 v34, v34, s66, v239
	v_pk_mul_f32 v[26:27], v[22:23], v[28:29]
	v_pk_add_f32 v[28:29], v[70:71], v[6:7]
	v_med3_f32 v35, v35, s66, v239
	v_min_f32_e32 v28, 0x40e00000, v28
	v_min_f32_e32 v29, 0x40e00000, v29
	v_pk_mul_f32 v[32:33], v[28:29], s[18:19] op_sel_hi:[1,0]
	v_pk_add_f32 v[22:23], v[72:73], v[8:9]
	v_exp_f32_e32 v32, v32
	v_exp_f32_e32 v33, v33
	v_pk_fma_f32 v[34:35], v[34:35], 4.0, 4.0 op_sel_hi:[1,0,0]
	v_pk_add_f32 v[30:31], v[108:109], v[4:5]
	v_pk_mul_f32 v[28:29], v[28:29], v[34:35]
	v_min_f32_e32 v34, 0x40e00000, v22
	v_min_f32_e32 v35, 0x40e00000, v23
	v_pk_mul_f32 v[22:23], v[34:35], s[18:19] op_sel_hi:[1,0]
	v_pk_add_f32 v[32:33], v[32:33], 1.0 op_sel_hi:[1,0]
	v_exp_f32_e32 v22, v22
	v_exp_f32_e32 v23, v23
	v_rcp_f32_e32 v32, v32
	v_rcp_f32_e32 v33, v33
	v_med3_f32 v30, v30, s66, v239
	v_pk_add_f32 v[22:23], v[22:23], 1.0 op_sel_hi:[1,0]
	v_med3_f32 v31, v31, s66, v239
	v_pk_mul_f32 v[28:29], v[28:29], v[32:33]
	v_rcp_f32_e32 v32, v22
	v_mov_b32_e32 v22, v199
	v_cvt_pk_fp8_f32 v22, v24, v25
	v_rcp_f32_e32 v33, v23
	v_mov_b32_e32 v23, v199
	v_pk_fma_f32 v[30:31], v[30:31], 4.0, 4.0 op_sel_hi:[1,0,0]
	v_cvt_pk_fp8_f32 v22, v26, v27 op_sel:[0,0,1]
	v_pk_add_f32 v[26:27], v[74:75], v[14:15]
	v_cvt_pk_fp8_f32 v23, v28, v29
	v_min_f32_e32 v26, 0x40e00000, v26
	v_min_f32_e32 v27, 0x40e00000, v27
	v_pk_mul_f32 v[24:25], v[34:35], v[30:31]
	v_pk_mul_f32 v[30:31], v[26:27], s[18:19] op_sel_hi:[1,0]
	v_pk_mul_f32 v[24:25], v[24:25], v[32:33]
	v_exp_f32_e32 v30, v30
	v_exp_f32_e32 v31, v31
	v_cvt_pk_fp8_f32 v23, v24, v25 op_sel:[0,0,1]
	v_pk_add_f32 v[24:25], v[76:77], v[16:17]
	v_pk_add_f32 v[32:33], v[114:115], v[10:11]
	v_min_f32_e32 v24, 0x40e00000, v24
	v_min_f32_e32 v25, 0x40e00000, v25
	v_pk_add_f32 v[30:31], v[30:31], 1.0 op_sel_hi:[1,0]
	v_pk_mul_f32 v[34:35], v[24:25], s[18:19] op_sel_hi:[1,0]
	v_rcp_f32_e32 v30, v30
	v_rcp_f32_e32 v31, v31
	v_exp_f32_e32 v34, v34
	v_exp_f32_e32 v35, v35
	v_med3_f32 v32, v32, s66, v239
	v_med3_f32 v33, v33, s66, v239
	v_pk_fma_f32 v[32:33], v[32:33], 4.0, 4.0 op_sel_hi:[1,0,0]
	v_pk_add_f32 v[28:29], v[116:117], v[12:13]
	v_pk_mul_f32 v[26:27], v[26:27], v[32:33]
	v_med3_f32 v28, v28, s66, v239
	v_pk_mul_f32 v[26:27], v[26:27], v[30:31]
	v_pk_add_f32 v[30:31], v[34:35], 1.0 op_sel_hi:[1,0]
	v_med3_f32 v29, v29, s66, v239
	v_rcp_f32_e32 v30, v30
	v_rcp_f32_e32 v31, v31
	v_pk_fma_f32 v[28:29], v[28:29], 4.0, 4.0 op_sel_hi:[1,0,0]
	v_med3_f32 v36, v36, s66, v239
	v_pk_mul_f32 v[24:25], v[24:25], v[28:29]
	v_med3_f32 v37, v37, s66, v239
	v_pk_mul_f32 v[28:29], v[24:25], v[30:31]
	v_pk_add_f32 v[30:31], v[78:79], v[6:7]
	v_pk_add_f32 v[24:25], v[80:81], v[8:9]
	v_min_f32_e32 v30, 0x40e00000, v30
	v_min_f32_e32 v31, 0x40e00000, v31
	v_pk_mul_f32 v[34:35], v[30:31], s[18:19] op_sel_hi:[1,0]
	v_pk_fma_f32 v[36:37], v[36:37], 4.0, 4.0 op_sel_hi:[1,0,0]
	v_exp_f32_e32 v34, v34
	v_exp_f32_e32 v35, v35
	v_pk_mul_f32 v[30:31], v[30:31], v[36:37]
	v_min_f32_e32 v36, 0x40e00000, v24
	v_min_f32_e32 v37, 0x40e00000, v25
	v_pk_mul_f32 v[24:25], v[36:37], s[18:19] op_sel_hi:[1,0]
	v_pk_add_f32 v[34:35], v[34:35], 1.0 op_sel_hi:[1,0]
	v_exp_f32_e32 v24, v24
	v_exp_f32_e32 v25, v25
	v_rcp_f32_e32 v34, v34
	v_rcp_f32_e32 v35, v35
	v_pk_add_f32 v[32:33], v[120:121], v[4:5]
	v_pk_add_f32 v[24:25], v[24:25], 1.0 op_sel_hi:[1,0]
	v_med3_f32 v32, v32, s66, v239
	v_pk_mul_f32 v[30:31], v[30:31], v[34:35]
	v_rcp_f32_e32 v34, v24
	v_rcp_f32_e32 v35, v25
	v_mov_b32_e32 v24, v199
	v_mov_b32_e32 v25, v199
	v_med3_f32 v33, v33, s66, v239
	v_cvt_pk_fp8_f32 v24, v26, v27
	v_cvt_pk_fp8_f32 v25, v30, v31
	v_pk_fma_f32 v[32:33], v[32:33], 4.0, 4.0 op_sel_hi:[1,0,0]
	v_add_u32_e32 v20, 0x80, v18
	v_pk_mul_f32 v[26:27], v[36:37], v[32:33]
	v_cvt_pk_fp8_f32 v24, v28, v29 op_sel:[0,0,1]
	v_pk_mul_f32 v[26:27], v[26:27], v[34:35]
	v_ashrrev_i32_e32 v21, 31, v20
	v_cvt_pk_fp8_f32 v25, v26, v27 op_sel:[0,0,1]
	v_lshlrev_b64 v[20:21], 10, v[20:21]
	v_lshl_add_u64 v[20:21], s[8:9], 0, v[20:21]
	v_permlane16_swap_b32_e32 v22, v24
	v_permlane16_swap_b32_e32 v23, v25
	v_lshl_add_u64 v[20:21], v[20:21], 0, v[198:199]
	global_store_dwordx4 v[20:21], v[22:25], off nt
	v_pk_add_f32 v[20:21], v[84:85], v[16:17]
	v_pk_add_f32 v[28:29], v[126:127], v[10:11]
	v_pk_add_f32 v[22:23], v[82:83], v[14:15]
	v_min_f32_e32 v20, 0x40e00000, v20
	v_min_f32_e32 v22, 0x40e00000, v22
	v_min_f32_e32 v23, 0x40e00000, v23
	v_pk_mul_f32 v[26:27], v[22:23], s[18:19] op_sel_hi:[1,0]
	v_min_f32_e32 v21, 0x40e00000, v21
	v_exp_f32_e32 v26, v26
	v_exp_f32_e32 v27, v27
	v_pk_mul_f32 v[30:31], v[20:21], s[18:19] op_sel_hi:[1,0]
	v_med3_f32 v28, v28, s66, v239
	v_exp_f32_e32 v30, v30
	v_pk_add_f32 v[26:27], v[26:27], 1.0 op_sel_hi:[1,0]
	v_exp_f32_e32 v31, v31
	v_rcp_f32_e32 v26, v26
	v_rcp_f32_e32 v27, v27
	v_med3_f32 v29, v29, s66, v239
	v_pk_fma_f32 v[28:29], v[28:29], 4.0, 4.0 op_sel_hi:[1,0,0]
	v_pk_add_f32 v[24:25], v[128:129], v[12:13]
	v_pk_mul_f32 v[22:23], v[22:23], v[28:29]
	v_med3_f32 v24, v24, s66, v239
	v_pk_mul_f32 v[22:23], v[22:23], v[26:27]
	v_pk_add_f32 v[26:27], v[30:31], 1.0 op_sel_hi:[1,0]
	v_med3_f32 v25, v25, s66, v239
	v_rcp_f32_e32 v26, v26
	v_rcp_f32_e32 v27, v27
	v_pk_fma_f32 v[24:25], v[24:25], 4.0, 4.0 op_sel_hi:[1,0,0]
	v_pk_add_f32 v[32:33], v[134:135], v[2:3]
	v_pk_mul_f32 v[20:21], v[20:21], v[24:25]
	v_med3_f32 v32, v32, s66, v239
	v_pk_mul_f32 v[24:25], v[20:21], v[26:27]
	v_pk_add_f32 v[26:27], v[86:87], v[6:7]
	v_med3_f32 v33, v33, s66, v239
	v_min_f32_e32 v26, 0x40e00000, v26
	v_min_f32_e32 v27, 0x40e00000, v27
	v_pk_mul_f32 v[30:31], v[26:27], s[18:19] op_sel_hi:[1,0]
	v_pk_add_f32 v[20:21], v[88:89], v[8:9]
	v_exp_f32_e32 v30, v30
	v_exp_f32_e32 v31, v31
	v_pk_fma_f32 v[32:33], v[32:33], 4.0, 4.0 op_sel_hi:[1,0,0]
	v_pk_add_f32 v[16:17], v[92:93], v[16:17]
	v_pk_mul_f32 v[26:27], v[26:27], v[32:33]
	v_min_f32_e32 v32, 0x40e00000, v20
	v_min_f32_e32 v33, 0x40e00000, v21
	v_pk_mul_f32 v[20:21], v[32:33], s[18:19] op_sel_hi:[1,0]
	v_pk_add_f32 v[30:31], v[30:31], 1.0 op_sel_hi:[1,0]
	v_exp_f32_e32 v20, v20
	v_exp_f32_e32 v21, v21
	v_rcp_f32_e32 v30, v30
	v_rcp_f32_e32 v31, v31
	v_min_f32_e32 v16, 0x40e00000, v16
	v_pk_add_f32 v[20:21], v[20:21], 1.0 op_sel_hi:[1,0]
	v_min_f32_e32 v17, 0x40e00000, v17
	v_pk_mul_f32 v[26:27], v[26:27], v[30:31]
	v_rcp_f32_e32 v30, v20
	v_mov_b32_e32 v20, v199
	v_cvt_pk_fp8_f32 v20, v22, v23
	v_pk_add_f32 v[28:29], v[136:137], v[4:5]
	v_rcp_f32_e32 v31, v21
	v_mov_b32_e32 v21, v199
	v_cvt_pk_fp8_f32 v20, v24, v25 op_sel:[0,0,1]
	v_pk_mul_f32 v[24:25], v[16:17], s[18:19] op_sel_hi:[1,0]
	v_med3_f32 v28, v28, s66, v239
	v_med3_f32 v29, v29, s66, v239
	v_cvt_pk_fp8_f32 v21, v26, v27
	v_exp_f32_e32 v24, v24
	v_exp_f32_e32 v25, v25
	v_pk_fma_f32 v[28:29], v[28:29], 4.0, 4.0 op_sel_hi:[1,0,0]
	v_pk_add_f32 v[10:11], v[138:139], v[10:11]
	v_pk_mul_f32 v[22:23], v[32:33], v[28:29]
	v_pk_add_f32 v[14:15], v[90:91], v[14:15]
	v_med3_f32 v10, v10, s66, v239
	v_med3_f32 v11, v11, s66, v239
	v_pk_mul_f32 v[22:23], v[22:23], v[30:31]
	v_min_f32_e32 v14, 0x40e00000, v14
	v_min_f32_e32 v15, 0x40e00000, v15
	v_pk_fma_f32 v[10:11], v[10:11], 4.0, 4.0 op_sel_hi:[1,0,0]
	v_cvt_pk_fp8_f32 v21, v22, v23 op_sel:[0,0,1]
	v_pk_mul_f32 v[22:23], v[14:15], s[18:19] op_sel_hi:[1,0]
	v_pk_mul_f32 v[10:11], v[14:15], v[10:11]
	v_pk_add_f32 v[14:15], v[24:25], 1.0 op_sel_hi:[1,0]
	v_pk_add_f32 v[12:13], v[140:141], v[12:13]
	v_rcp_f32_e32 v14, v14
	v_rcp_f32_e32 v15, v15
	v_med3_f32 v12, v12, s66, v239
	v_med3_f32 v13, v13, s66, v239
	v_pk_fma_f32 v[12:13], v[12:13], 4.0, 4.0 op_sel_hi:[1,0,0]
	v_pk_add_f32 v[6:7], v[94:95], v[6:7]
	v_pk_mul_f32 v[12:13], v[16:17], v[12:13]
	v_min_f32_e32 v6, 0x40e00000, v6
	v_min_f32_e32 v7, 0x40e00000, v7
	v_pk_mul_f32 v[12:13], v[12:13], v[14:15]
	v_pk_mul_f32 v[14:15], v[6:7], s[18:19] op_sel_hi:[1,0]
	v_pk_add_f32 v[2:3], v[146:147], v[2:3]
	v_exp_f32_e32 v22, v22
	v_exp_f32_e32 v23, v23
	v_exp_f32_e32 v14, v14
	v_exp_f32_e32 v15, v15
	v_med3_f32 v2, v2, s66, v239
	v_med3_f32 v3, v3, s66, v239
	v_pk_add_f32 v[8:9], v[96:97], v[8:9]
	v_pk_fma_f32 v[2:3], v[2:3], 4.0, 4.0 op_sel_hi:[1,0,0]
	v_pk_add_f32 v[22:23], v[22:23], 1.0 op_sel_hi:[1,0]
	v_pk_mul_f32 v[2:3], v[6:7], v[2:3]
	v_min_f32_e32 v6, 0x40e00000, v8
	v_min_f32_e32 v7, 0x40e00000, v9
	v_pk_mul_f32 v[8:9], v[6:7], s[18:19] op_sel_hi:[1,0]
	v_pk_add_f32 v[14:15], v[14:15], 1.0 op_sel_hi:[1,0]
	v_exp_f32_e32 v8, v8
	v_exp_f32_e32 v9, v9
	v_rcp_f32_e32 v22, v22
	v_rcp_f32_e32 v23, v23
	v_rcp_f32_e32 v14, v14
	v_rcp_f32_e32 v15, v15
	v_pk_add_f32 v[8:9], v[8:9], 1.0 op_sel_hi:[1,0]
	v_pk_mul_f32 v[10:11], v[10:11], v[22:23]
	v_pk_add_f32 v[4:5], v[148:149], v[4:5]
	v_pk_mul_f32 v[2:3], v[2:3], v[14:15]
	v_rcp_f32_e32 v8, v8
	v_rcp_f32_e32 v9, v9
	v_mov_b32_e32 v22, v199
	v_mov_b32_e32 v23, v199
	v_med3_f32 v4, v4, s66, v239
	v_med3_f32 v5, v5, s66, v239
	v_cvt_pk_fp8_f32 v22, v10, v11
	v_cvt_pk_fp8_f32 v23, v2, v3
	v_pk_fma_f32 v[4:5], v[4:5], 4.0, 4.0 op_sel_hi:[1,0,0]
	s_andn2_b64 vcc, exec, s[24:25]
	v_pk_mul_f32 v[2:3], v[6:7], v[4:5]
	v_cvt_pk_fp8_f32 v22, v12, v13 op_sel:[0,0,1]
	v_pk_mul_f32 v[2:3], v[2:3], v[8:9]
	s_mov_b64 s[24:25], -1
	v_cvt_pk_fp8_f32 v23, v2, v3 op_sel:[0,0,1]
	v_add_u32_e32 v2, 0xa0, v18
	v_ashrrev_i32_e32 v3, 31, v2
	v_lshlrev_b64 v[2:3], 10, v[2:3]
	v_lshl_add_u64 v[2:3], s[8:9], 0, v[2:3]
	v_permlane16_swap_b32_e32 v20, v22
	v_permlane16_swap_b32_e32 v21, v23
	v_lshl_add_u64 v[2:3], v[2:3], 0, v[198:199]
	global_store_dwordx4 v[2:3], v[20:23], off nt
	s_cbranch_vccnz .LBB0_1076
	s_andn2_b64 vcc, exec, s[6:7]
	s_cbranch_vccnz .LBB0_1075
	s_barrier
	s_branch .LBB0_1075
